# v13 variant: half of layer-0 gate/up piggyback work moved to the layer-0 down GEMM
# speedup vs baseline: 1.0068x; 1.0068x over previous
; template <class Epi, class Sched>
; __device__ __forceinline__ void gemm_phase(LAS unsigned char* lds, const int K, const Sched& S, const Epi& E) {
;     const int tid = tid_fresh(), wid = __builtin_amdgcn_readfirstlane(tid >> 6), lane = tid & 63, wr = wid >> 2, wc = wid & 3, fr = lane & 15, fq = lane >> 4;
;     const int nt = K / BK;
;     int R0, C0, R1, C1; stage_rc(tid * 16, R0, C0); stage_rc(tid * 16 + 8192, R1, C1);
;     const int Rb0 = Epi::PERM ? ((R0 & ~31) + perm32(R0 & 31)) : R0, Rb1 = Epi::PERM ? ((R1 & ~31) + perm32(R1 & 31)) : R1;
;     const unsigned voffB0 = S.b_off(Rb0, C0), voffB1 = S.b_off(Rb1, C1);
;     const size_t kstep = (size_t)(BK * 2);
;     const size_t kstepB = S.b_kstep(), hstep = S.b_hstep();
;     const unsigned ldsw = (unsigned)wid * 1024u;
;     const int aoff = lds_byte(wr * 64 + fr, fq * 8), boff = lds_byte(wc * 32 + fr, fq * 8);
;     ...
;     Unit cur, nxt; int ui = 0;
;     if (!S.next(0, cur)) return;
;     f32x4 acc[2][2][4][2];
; #pragma unroll
;     for (int a = 0; a < 2; ++a)
; #pragma unroll
;         for (int b = 0; b < 2; ++b)
; #pragma unroll
;             for (int m = 0; m < 4; ++m)
; #pragma unroll
;                 for (int n = 0; n < 2; ++n) acc[a][b][m][n] = (f32x4){0.f, 0.f, 0.f, 0.f};
;     bf16x8 At[4][2], B0[2][2], B1[2][2];
;     const char* const gA = S.a_base();
;     unsigned c00, c01, c10, c11, n00, n01, n10, n11;
;     PG8_AOFFS(cur, c00, c01, c10, c11);
;     const char* cB = S.b_ptr(cur);
;     PG8_STAGE(PG8_SB(0, 0), cB, voffB0, voffB1); PG8_STAGE(PG8_SA(0, 0), gA, c00, c01); PG8_STAGE(PG8_SB(0, 1), cB + hstep, voffB0, voffB1); PG8_STAGE(PG8_SA(0, 1), gA, c10, c11);
;     if (wr == 1) PG8_BAR;
;     PG8_WAIT_V(4); PG8_BAR;
;     PG8_STAGE(PG8_SB(1, 0), cB + kstepB, voffB0, voffB1); PG8_STAGE(PG8_SA(1, 0), gA + kstep, c00, c01); PG8_STAGE(PG8_SB(1, 1), cB + hstep + kstepB, voffB0, voffB1);
;     __device__ __forceinline__ bool next(int i, Unit& u) const {
;         const int L = i * G + c; if (L >= ntiles * 8) return false;
;         const int rt = L >> 3; u.pn = L & 7; u.e = tile_e[rt]; u.pm = rt - tstart[u.e]; u.rbase = (u.e < NE) ? rt * BM : SLOT_SH + u.pm * BM; return true;
;     }
;     __device__ __forceinline__ const char* a_base() const { return (const char*)A; }
;     __device__ __forceinline__ unsigned a_off(const Unit& u, int r) const { return (unsigned)((u.rbase + r) * FF) * 2u; }
.LBB0_1152:
	s_or_b64 exec, exec, s[0:1]
	v_readlane_b32 s0, v254, 0
	v_readlane_b32 s2, v254, 5
	v_readlane_b32 s1, v254, 1
	s_lshl_b32 s15, s28, 3
	s_and_b32 s3, s2, 7
	v_mov_b32_e32 v2, v0
	s_waitcnt lgkmcnt(0)
	s_barrier
	v_readlane_b32 s84, v254, 0
	v_readlane_b32 s85, v254, 1
	s_nop 1
	s_load_dwordx2 s[74:75], s[84:85], 0xd8
	s_load_dwordx2 s[76:77], s[84:85], 0xe0
	s_load_dwordx2 s[78:79], s[84:85], 0x118
	v_and_b32_e32 v252, 63, v0
	v_lshrrev_b32_e32 v253, 6, v0
	v_lshlrev_b32_e32 v238, 2, v252
	v_lshlrev_b32_e32 v252, 4, v252
	v_add_u32_e32 v239, 0x800, v238
	v_add_u32_e32 v240, 0x1000, v238
	v_add_u32_e32 v241, 0x1800, v238
	v_readlane_b32 s86, v254, 4
	v_readlane_b32 s87, v255, 40
	v_readfirstlane_b32 s88, v253
	s_nop 3
	s_lshl_b32 s71, s86, 3
	s_lshl_b32 s87, s87, 3
	s_add_u32 s87, s87, s88
	s_add_u32 s70, s87, 0x20000
	s_mov_b32 s80, 0
	s_mov_b32 s82, 0
	s_mov_b32 s90, 0
	s_waitcnt lgkmcnt(0)
	v_writelane_b32 v254, s3, 39
	s_cmp_lt_i32 s2, s15
	s_nop 0
	v_readfirstlane_b32 s33, v2
	s_cbranch_scc0 .LBB0_1166
	v_ashrrev_i32_e32 v1, 31, v2
	v_lshrrev_b32_e32 v1, 26, v1
	v_add_u32_e32 v1, v2, v1
	v_ashrrev_i32_e32 v4, 6, v1
	v_bfe_i32 v1, v2, 27, 1
	v_lshlrev_b32_e32 v3, 4, v2
	v_lshrrev_b32_e32 v1, 22, v1
	v_add_u32_e32 v1, v3, v1
	v_and_b32_e32 v1, 0xfffffc00, v1
	v_sub_u32_e32 v1, v3, v1
	v_lshrrev_b32_e32 v5, 4, v1
	v_bitop3_b32 v5, v5, v1, 32 bitop3:0x6c
	v_ashrrev_i32_e32 v1, 31, v1
	v_lshrrev_b32_e32 v1, 26, v1
	v_lshlrev_b32_e32 v6, 3, v4
	v_add_u32_e32 v1, v5, v1
	v_and_b32_e32 v6, -16, v6
	v_ashrrev_i32_e32 v7, 6, v1
	v_add_u32_e32 v3, 0x2000, v3
	v_add_u32_e32 v1, v7, v6
	v_ashrrev_i32_e32 v6, 31, v3
	v_lshrrev_b32_e32 v6, 22, v6
	v_add_u32_e32 v6, v3, v6
	s_load_dwordx2 s[0:1], s[0:1], 0x118
	v_ashrrev_i32_e32 v6, 10, v6
	v_mul_i32_i24_e32 v8, 0x400, v6
	v_sub_u32_e32 v3, v3, v8
	v_lshrrev_b32_e32 v8, 4, v3
	v_bitop3_b32 v3, v8, v3, 32 bitop3:0x6c
	s_waitcnt lgkmcnt(0)
	s_add_u32 s2, s0, 0x3ee90000
	v_ashrrev_i32_e32 v9, 31, v3
	s_addc_u32 s3, s1, 0
	v_lshrrev_b32_e32 v9, 26, v9
	s_add_u32 s46, s0, 0x24830000
	v_add_u32_e32 v9, v3, v9
	s_addc_u32 s47, s1, 0
	s_ashr_i32 s11, s33, 6
	v_lshlrev_b32_e32 v8, 3, v6
	v_ashrrev_i32_e32 v10, 6, v9
	v_readlane_b32 s4, v254, 39
	v_and_b32_e32 v9, 0xc0, v9
	s_ashr_i32 s10, s33, 8
	v_and_b32_e32 v8, -16, v8
	s_lshl_b32 s48, s11, 10
	s_lshl_b32 s4, s4, 12
	v_lshlrev_b32_e32 v6, 5, v6
	v_sub_u32_e32 v3, v3, v9
	v_mov_b32_e32 v9, 1
	v_add_u32_e32 v146, v10, v8
	s_add_u32 s8, s46, s4
	v_readlane_b32 s4, v254, 5
	v_and_b32_e32 v6, 32, v6
	v_ashrrev_i16_sdwa v3, v9, sext(v3) dst_sel:DWORD dst_unused:UNUSED_PAD src0_sel:DWORD src1_sel:BYTE_0
	s_addc_u32 s9, s47, 0
	s_ashr_i32 s12, s4, 3
	v_and_b32_e32 v8, 3, v10
	s_mov_b32 s5, 0xfffffe0
	v_lshlrev_b32_e32 v10, 1, v146
	v_lshrrev_b32_e32 v11, 2, v146
	v_add_u32_sdwa v3, v6, sext(v3) dst_sel:DWORD dst_unused:UNUSED_PAD src0_sel:DWORD src1_sel:WORD_0
	s_lshl_b32 s4, s12, 2
	v_and_or_b32 v8, v146, s5, v8
	v_and_b32_e32 v10, 24, v10
	v_and_b32_e32 v11, 4, v11
	v_lshlrev_b32_e32 v6, 8, v3
	s_add_i32 s4, s4, 0
	v_or3_b32 v8, v8, v10, v11
	v_and_b32_e32 v6, 0xffff800, v6
	s_add_i32 s4, s4, 0x21160
	v_add_lshl_u32 v130, v8, v6, 4
	v_and_b32_e32 v6, 3, v7
	v_mul_i32_i24_e32 v7, 64, v7
	v_sub_u32_e32 v5, v5, v7
	v_mov_b32_e32 v7, s4
	ds_read_b32 v7, v7
	v_lshlrev_b32_e32 v8, 1, v1
	v_lshrrev_b32_e32 v10, 2, v1
	v_and_or_b32 v6, v1, s5, v6
	v_and_b32_e32 v8, 24, v8
	v_and_b32_e32 v10, 4, v10
	v_or3_b32 v6, v6, v8, v10
	s_waitcnt lgkmcnt(0)
	v_lshlrev_b32_e32 v8, 2, v7
	v_add_u32_e32 v8, 0, v8
	v_add_u32_e32 v8, 0x21040, v8
	ds_read_b32 v8, v8
	s_lshl_b32 s13, s12, 8
	v_readfirstlane_b32 s4, v7
	s_ashr_i32 s5, s4, 31
	v_lshlrev_b32_e32 v4, 5, v4
	s_waitcnt lgkmcnt(0)
	v_readfirstlane_b32 s14, v8
	s_sub_i32 s12, s12, s14
	s_lshl_b32 s12, s12, 8
	v_cmp_lt_i64_e64 s[6:7], s[4:5], 64
	s_add_i32 s12, s12, 0xff00
	v_and_b32_e32 v4, 32, v4
	v_ashrrev_i16_sdwa v5, v9, sext(v5) dst_sel:DWORD dst_unused:UNUSED_PAD src0_sel:DWORD src1_sel:BYTE_0
	s_and_b64 s[6:7], s[6:7], exec
	v_add_u32_sdwa v4, v4, sext(v5) dst_sel:DWORD dst_unused:UNUSED_PAD src0_sel:DWORD src1_sel:WORD_0
	s_cselect_b32 s12, s13, s12
	s_lshl_b64 s[4:5], s[4:5], 21
	v_lshlrev_b32_e32 v5, 8, v4
	s_add_u32 s38, s8, s4
	v_and_b32_e32 v5, 0xffff800, v5
	s_addc_u32 s39, s9, s5
	s_add_i32 s49, s48, 0
	v_add_lshl_u32 v132, v6, v5, 4
	s_add_i32 m0, s49, 0x10000
	v_add_u32_e32 v5, s12, v1
	v_lshlrev_b32_e32 v149, 1, v4
	v_mov_b32_e32 v135, 0
	global_load_lds_dwordx4 v132, s[38:39]
	s_add_i32 m0, s49, 0x12000
	v_add_u32_e32 v6, s12, v146
	v_add_u32_e32 v147, 0x80, v1
	v_lshl_add_u32 v134, v5, 10, v149
	v_lshlrev_b32_e32 v150, 1, v3
	v_mov_b32_e32 v133, v135
	global_load_lds_dwordx4 v130, s[38:39]
	s_mov_b32 m0, s49
	s_add_i32 s50, s49, 0x2000
	v_add_u32_e32 v7, s12, v147
	v_lshl_add_u32 v136, v6, 10, v150
	v_lshl_add_u64 v[4:5], s[38:39], 0, v[132:133]
	v_mov_b32_e32 v131, v135
	global_load_lds_dwordx4 v134, s[2:3]
	s_mov_b32 m0, s50
	s_mov_b64 s[4:5], 0x800
	v_lshl_add_u32 v138, v7, 10, v149
	v_lshl_add_u64 v[6:7], s[38:39], 0, v[130:131]
	global_load_lds_dwordx4 v136, s[2:3]
	v_lshl_add_u64 v[4:5], v[4:5], 0, s[4:5]
	s_add_i32 m0, s49, 0x14000
	v_add_u32_e32 v148, 0x80, v146
	global_load_lds_dwordx4 v[4:5], off
	v_lshl_add_u64 v[4:5], v[6:7], 0, s[4:5]
	s_add_i32 m0, s49, 0x16000
	s_add_i32 s51, s49, 0x4000
	v_add_u32_e32 v8, s12, v148
	global_load_lds_dwordx4 v[4:5], off
	s_mov_b32 m0, s51
	s_add_i32 s52, s49, 0x6000
	v_lshl_add_u32 v140, v8, 10, v150
	global_load_lds_dwordx4 v138, s[2:3]
	s_mov_b32 m0, s52
	s_mov_b32 s53, 0
	global_load_lds_dwordx4 v140, s[2:3]
	s_mov_b32 s54, 0x10000
	s_cmp_lg_u32 s10, 1
	v_mov_b32_e32 v137, v135
	s_cbranch_scc1 .LBB0_1155
	s_barrier

; #define PG8_STAGE(bufoff, gbase, v0, v1) do { \
;         __builtin_amdgcn_global_load_lds((const unsigned*)((const char*)(gbase) + (v0)), (LAS unsigned*)(lds + (bufoff) + ldsw), 16, 0, 0); \
;         __builtin_amdgcn_global_load_lds((const unsigned*)((const char*)(gbase) + (v1)), (LAS unsigned*)(lds + (bufoff) + ldsw + 8192), 16, 0, 0); } while (0)
; #define PG8_LDA(dst, b, h) do { _Pragma("unroll") for (int m = 0; m < 4; ++m) _Pragma("unroll") for (int k = 0; k < 2; ++k) dst[m][k] = *(const LAS bf16x8*)(lds + PG8_SA(b, h) + aoff + m * 2048 + k * 1024); } while (0)
; #define PG8_LDB(dst, b, h) do { _Pragma("unroll") for (int n = 0; n < 2; ++n) _Pragma("unroll") for (int k = 0; k < 2; ++k) dst[n][k] = *(const LAS bf16x8*)(lds + PG8_SB(b, h) + boff + n * 2048 + k * 1024); } while (0)
; #define PG8_MMA(ai, bj, At, Bt) do { __builtin_amdgcn_s_setprio(1); _Pragma("unroll") for (int m = 0; m < 4; ++m) _Pragma("unroll") for (int n = 0; n < 2; ++n) _Pragma("unroll") for (int k = 0; k < 2; ++k) \
;         acc[ai][bj][m][n] = __builtin_amdgcn_mfma_f32_16x16x32_bf16(Bt[n][k], At[m][k], acc[ai][bj][m][n], 0, 0, 0); __builtin_amdgcn_s_setprio(0); } while (0)
; #define PG8_WAIT_V(n) asm volatile("s_waitcnt vmcnt(" #n ")" ::: "memory")
; #define PG8_BAR __builtin_amdgcn_s_barrier()
; #define PG8_SCHED __builtin_amdgcn_sched_barrier(0)
; template <class Epi, class Sched>
; __device__ __forceinline__ void gemm_phase(LAS unsigned char* lds, const int K, const Sched& S, const Epi& E) {
;     ...
;             PG8_WAIT_V(6); PG8_BAR; PG8_MMA(1, 1, At, B1); PG8_BAR;
;             PG8_LDB(B0, 1, 0); PG8_SCHED; PG8_LDA(At, 1, 0); PG8_STAGE(PG8_SA(0, 1), a2, x10, x11);
; __device__ __forceinline__ bool bg_decode(int st, int wg, int NW, int lane, KP kp, const float*& src, int& ldS, bf16_t*& dst, int& o2) {
;     ...
;     if (r < 65536) {
;         const int e = r >> 10, kc = (r >> 2) & 255, kind = (r >> 1) & 1, cc = r & 1, n = cc * 256 + lane;
;         ldS = FF; o2 = 256 * 8;
;         src = kp->in[27 + kind] + ((size_t)(l * NE + e) * D + kc * 8) * FF + n;
;         const int drow = (n >> 7) * 256 + kind * 128 + (n & 127);
;         dst = (bf16_t*)(ws + WS_WGU) + l * WGU_L + (size_t)e * 1024 * D + ((size_t)kc * 1024 + drow) * 8;
.Lpb9_p4j:
	s_barrier
	s_setprio 1
	v_mfma_f32_16x16x32_bf16 v[54:57], v[216:219], v[180:183], v[54:57]
	v_mfma_f32_16x16x32_bf16 v[50:53], v[224:227], v[180:183], v[50:53]
	v_mfma_f32_16x16x32_bf16 v[38:41], v[216:219], v[188:191], v[38:41]
	v_mfma_f32_16x16x32_bf16 v[34:37], v[224:227], v[188:191], v[34:37]
	v_mfma_f32_16x16x32_bf16 v[22:25], v[216:219], v[196:199], v[22:25]
	v_mfma_f32_16x16x32_bf16 v[18:21], v[224:227], v[196:199], v[18:21]
	v_mfma_f32_16x16x32_bf16 v[6:9], v[216:219], v[208:211], v[6:9]
	v_mfma_f32_16x16x32_bf16 v[2:5], v[224:227], v[208:211], v[2:5]
	v_mfma_f32_16x16x32_bf16 v[54:57], v[220:223], v[184:187], v[54:57]
	v_mfma_f32_16x16x32_bf16 v[50:53], v[228:231], v[184:187], v[50:53]
	v_mfma_f32_16x16x32_bf16 v[38:41], v[220:223], v[192:195], v[38:41]
	v_mfma_f32_16x16x32_bf16 v[34:37], v[228:231], v[192:195], v[34:37]
	v_mfma_f32_16x16x32_bf16 v[22:25], v[220:223], v[200:203], v[22:25]
	v_mfma_f32_16x16x32_bf16 v[18:21], v[228:231], v[200:203], v[18:21]
	v_mfma_f32_16x16x32_bf16 v[6:9], v[220:223], v[212:215], v[6:9]
	v_mfma_f32_16x16x32_bf16 v[2:5], v[228:231], v[212:215], v[2:5]
	s_setprio 0
	s_add_i32 s67, 0, 0x18000
	v_add_u32_e32 v134, s67, v151
	s_barrier
	ds_read_b128 v[164:167], v134
	ds_read_b128 v[168:171], v134 offset:1024
	ds_read_b128 v[172:175], v134 offset:2048
	ds_read_b128 v[176:179], v134 offset:3072
	s_mov_b32 m0, s51
	ds_read_b128 v[180:183], v154 offset:32768
	ds_read_b128 v[184:187], v154 offset:33792
	ds_read_b128 v[188:191], v154 offset:34816
	ds_read_b128 v[192:195], v154 offset:35840
	ds_read_b128 v[196:199], v154 offset:36864
	ds_read_b128 v[200:203], v154 offset:37888
	ds_read_b128 v[208:211], v154 offset:38912
	ds_read_b128 v[212:215], v154 offset:39936
	v_cndmask_b32_e32 v134, v140, v160, vcc
	global_load_lds_dwordx4 v139, s[44:45]
	s_mov_b32 m0, s52
	s_nop 0
	global_load_lds_dwordx4 v134, s[44:45]
	s_cmp_ge_u32 s70, 0x24000
	s_cbranch_scc1 .Lpb9_p5n
	s_cmp_eq_u32 s80, 0
	s_cbranch_scc0 .Lpb9_adv2
	s_cmp_ge_u32 s70, 0x18000
	s_cselect_b32 s84, 0x18000, 0
	s_cselect_b32 s83, 0x10000000, 0
	s_mov_b32 s81, 0x4030000
	s_cselect_b32 s81, 0x14430000, s81
	s_sub_u32 s84, s70, s84
	s_lshr_b32 s85, s84, 2
	s_lshl_b32 s85, s85, 14
	s_and_b32 s86, s84, 1
	s_lshl_b32 s87, s86, 10
	s_add_u32 s87, s87, s85
	s_add_u32 s87, s87, s83
	s_bitcmp1_b32 s84, 1
	s_cselect_b64 s[72:73], s[76:77], s[74:75]
	s_add_u32 s72, s72, s87
	s_addc_u32 s73, s73, 0
	s_add_u32 s88, s72, 0x2000
	s_addc_u32 s89, s73, 0
	s_lshl_b32 s86, s86, 13
	s_add_u32 s85, s85, s86
	s_and_b32 s86, s84, 2
	s_lshl_b32 s86, s86, 10
	s_add_u32 s85, s85, s86
	s_add_u32 s85, s85, s81
	v_add_u32_e32 v253, s85, v252
	s_movk_i32 s81, 0x400
	s_branch .Lpb9_ld2

; __device__ __forceinline__ bool bg_decode(int st, int wg, int NW, int lane, KP kp, const float*& src, int& ldS, bf16_t*& dst, int& o2) {
;     ...
;     if (r < 65536) {
;         const int e = r >> 10, kc = (r >> 2) & 255, kind = (r >> 1) & 1, cc = r & 1, n = cc * 256 + lane;
;         ldS = FF; o2 = 256 * 8;
;         src = kp->in[27 + kind] + ((size_t)(l * NE + e) * D + kc * 8) * FF + n;
;         const int drow = (n >> 7) * 256 + kind * 128 + (n & 127);
;         dst = (bf16_t*)(ws + WS_WGU) + l * WGU_L + (size_t)e * 1024 * D + ((size_t)kc * 1024 + drow) * 8;
.Lpb9_d1:
	s_cmp_ge_u32 s70, 0x24000
	s_cbranch_scc1 .Lpb9_dend
	s_cmp_eq_u32 s80, 0
	s_cbranch_scc0 .Lpb9_adv1
	s_cmp_ge_u32 s70, 0x18000
	s_cselect_b32 s84, 0x18000, 0
	s_cselect_b32 s83, 0x10000000, 0
	s_mov_b32 s81, 0x4030000
	s_cselect_b32 s81, 0x14430000, s81
	s_sub_u32 s84, s70, s84
	s_lshr_b32 s85, s84, 2
	s_lshl_b32 s85, s85, 14
	s_and_b32 s86, s84, 1
	s_lshl_b32 s87, s86, 10
	s_add_u32 s87, s87, s85
	s_add_u32 s87, s87, s83
	s_bitcmp1_b32 s84, 1
	s_cselect_b64 s[72:73], s[76:77], s[74:75]
	s_add_u32 s72, s72, s87
	s_addc_u32 s73, s73, 0
	s_add_u32 s88, s72, 0x2000
	s_addc_u32 s89, s73, 0
	s_lshl_b32 s86, s86, 13
	s_add_u32 s85, s85, s86
	s_and_b32 s86, s84, 2
	s_lshl_b32 s86, s86, 10
	s_add_u32 s85, s85, s86
	s_add_u32 s85, s85, s81
	v_add_u32_e32 v253, s85, v252
	s_movk_i32 s81, 0x400
	s_branch .Lpb9_ld1
